# gdnprep stage A: the first unit's two small-array loads requested before the q/k norm pass (later units were already requested one unit ahead)
# baseline (speedup 1.0000x reference)
; DI int tidx() { int t = threadIdx.x & 255; asm volatile("" : "+v"(t)); return t; }
; DI float bflo(unsigned u) { return __uint_as_float(u << 16); }
; DI float bfhi(unsigned u) { return __uint_as_float(u & 0xffff0000u); }
; DI void phase_qknorm(const Params& p, int bid, int nb) {
;   const int lane = tidx() & 63, gw = bid * 4 + (tidx() >> 6), nw = nb * 4;
;   const bf16_t* proj = (const bf16_t*)(p.ws + WS_P);
;   unsigned* qk = (unsigned*)(p.ws + WS_CTL) + 64;
;   for (int it = gw; it < 4096; it += nw) {
;     const int bh = it >> 7, j = it & 127, b = bh >> 3, h = bh & 7;
;     const bf16_t* rp = proj + ((size_t)b * S_ + j * 64 + lane) * PP + h * 64;
;     float sq = 0.f, sk = 0.f;
; #pragma unroll
;     for (int q = 0; q < 8; ++q) { const u32x4 wq = *(const u32x4*)(rp + 8 * q), wk = *(const u32x4*)(rp + 512 + 8 * q);
; #pragma unroll
;       for (int e = 0; e < 4; ++e) { const float a0 = bflo(wq[e]), a1 = bfhi(wq[e]), c0 = bflo(wk[e]), c1 = bfhi(wk[e]); sq += a0 * a0 + a1 * a1; sk += c0 * c0 + c1 * c1; } }
; #pragma unroll
;     for (int d = 32; d >= 1; d >>= 1) { sq = fmaxf(sq, __shfl_xor(sq, d)); sk = fmaxf(sk, __shfl_xor(sk, d)); }
; DI void gdn_prep_unit(const Params& p, int U, char* lds) {
;     ...
;     const float g = small[(t0 + lane) * 16 + 12 + h], bt = small[(t0 + lane) * 16 + 8 + h];
.LBB0_1081:
	v_cmp_gt_u32_e32 vcc, 64, v206
	s_and_saveexec_b64 s[14:15], vcc
	v_and_b32_e32 v246, 0x7f, v176
	v_lshlrev_b32_e32 v246, 6, v246
	v_or_b32_e32 v246, v246, v206
	v_lshlrev_b32_e32 v246, 6, v246
	v_bfe_u32 v247, v176, 7, 2
	v_lshl_add_u32 v246, v247, 2, v246
	s_add_u32 s12, s84, 0x1700000
	s_addc_u32 s13, s85, 0
	global_load_dword v244, v246, s[12:13] offset:48
	global_load_dword v245, v246, s[12:13] offset:32
	s_or_b64 exec, exec, s[14:15]
	s_mov_b32 s6, 1
	v_mov_b32_e32 v0, v206
	v_mov_b32_e32 v1, v206
	s_movk_i32 s0, 0x1000
	v_ashrrev_i32_e32 v1, 6, v1
	v_lshl_add_u32 v17, v176, 2, v1
	v_cmp_gt_i32_e32 vcc, s0, v17
	s_and_saveexec_b64 s[4:5], vcc
	s_cbranch_execz .LBB0_1086
	v_and_b32_e32 v16, 63, v0
	v_mbcnt_hi_u32_b32 v0, -1, v177
	v_and_b32_e32 v1, 64, v0
	v_add_u32_e32 v1, 64, v1
	v_xor_b32_e32 v2, 32, v0
	v_cmp_lt_i32_e64 s[0:1], v2, v1
	s_lshl_b32 s2, s86, 3
	v_mov_b32_e32 v19, 0
	v_cndmask_b32_e64 v2, v0, v2, s[0:1]
	v_lshlrev_b32_e32 v24, 2, v2
	v_xor_b32_e32 v2, 16, v0
	v_cmp_lt_i32_e64 s[0:1], v2, v1
	v_cmp_eq_u32_e32 vcc, 0, v16
	v_lshlrev_b32_e32 v30, 6, v17
	v_cndmask_b32_e64 v2, v0, v2, s[0:1]
	v_lshlrev_b32_e32 v25, 2, v2
	v_xor_b32_e32 v2, 8, v0
	v_cmp_lt_i32_e64 s[0:1], v2, v1
	s_lshl_b32 s3, s86, 9
	s_mov_b64 s[8:9], 0
	v_cndmask_b32_e64 v2, v0, v2, s[0:1]
	v_lshlrev_b32_e32 v26, 2, v2
	v_xor_b32_e32 v2, 4, v0
	v_cmp_lt_i32_e64 s[0:1], v2, v1
	s_movk_i32 s10, 0x2c00
	v_mov_b64_e32 v[20:21], s[58:59]
	v_cndmask_b32_e64 v2, v0, v2, s[0:1]
	v_lshlrev_b32_e32 v27, 2, v2
	v_xor_b32_e32 v2, 2, v0
	v_cmp_lt_i32_e64 s[0:1], v2, v1
	s_movk_i32 s11, 0xfff
	s_nop 0
	v_cndmask_b32_e64 v2, v0, v2, s[0:1]
	v_lshlrev_b32_e32 v28, 2, v2
	v_xor_b32_e32 v2, 1, v0
	v_cmp_lt_i32_e64 s[0:1], v2, v1
	s_nop 1
	v_cndmask_b32_e64 v0, v0, v2, s[0:1]
	v_lshlrev_b32_e32 v29, 2, v0
	s_branch .LBB0_1084
